# PROJ GEMM: next unit's A11 stage issued before epilogue stores; peeled first K-loop body with vmcnt relaxed past the stores
# baseline (speedup 1.0000x reference)
;     __device__ bool next(int i, Unit& u) const { const long L = (long)i * G + c; if (L >= nwg) return false; tile_of((int)L, nM, nN, u.pm, u.pn, wgm); u.z = 0; return true; }
; #define PG8_STAGE(bufoff, gbase, voff) do { _Pragma("unroll") for (int _i = 0; _i < 2; ++_i) \
;         __builtin_amdgcn_global_load_lds((const unsigned*)((const char*)(gbase) + (voff)[_i]), (PG8_LAS unsigned*)(lds + (bufoff) + ldsw + _i * 8192), 16, 0, 0); } while (0)
; #define PG8_WAIT_V(n) asm volatile("s_waitcnt vmcnt(" #n ")" ::: "memory")
; #define PG8_BAR __builtin_amdgcn_s_barrier()
;     __device__ bool next(int i, Unit& u) const { const int j = i / 6, r = i - 6 * j; const long L = (long)j * G + c; if (L >= nwg) return false; tile_of((int)L, nM, nN, u.pm, u.pn, wgm); u.z = (r >> 1) + 4 * (r & 1); return true; }
; #define PG8_STAGE(bufoff, gbase, voff) do { _Pragma("unroll") for (int _i = 0; _i < 2; ++_i) \
;         __builtin_amdgcn_global_load_lds((const unsigned*)((const char*)(gbase) + (voff)[_i]), (PG8_LAS unsigned*)(lds + (bufoff) + ldsw + _i * 8192), 16, 0, 0); } while (0)
; #define PG8_BAR __builtin_amdgcn_s_barrier()
; template <class Epi, class Sched, bool ALIGN_EPI = true>
; __device__ __forceinline__ void gemm_phase(PG8_LAS unsigned char* lds, const Gemm g, const Sched& S, const Epi& E) {
;     ...
;     const int aoff = lds_byte(wr * 64 + fr, fq * 8), boff = lds_byte(wc * 32 + fr, fq * 8);
;     ...
;     Unit cur, nxt; int ui = 0;
;     if (!S.next(0, cur)) return;
;     f32x4 acc[2][2][4][2];
; #pragma unroll
;     for (int a = 0; a < 2; ++a)
; #pragma unroll
;         for (int b = 0; b < 2; ++b)
; #pragma unroll
;             for (int m = 0; m < 4; ++m)
; #pragma unroll
;                 for (int n = 0; n < 2; ++n) acc[a][b][m][n] = (f32x4){0.f, 0.f, 0.f, 0.f};
;     s16x8 At[4][2], B0[2][2], B1[2][2];
;     const char* cA = (const char*)(g.A + (long)cur.z * g.zA) + (size_t)cur.pm * tA; const char* cB = (const char*)(g.Bt + (long)cur.z * g.zB) + (size_t)cur.pn * tB;
;     PG8_STAGE(PG8_SB(0, 0), cB, voffB); PG8_STAGE(PG8_SB(0, 1), cB + hB, voffB); PG8_STAGE(PG8_SA(0, 0), cA, voffA); PG8_STAGE(PG8_SA(0, 1), cA + hA, voffA);
;     if (wr == 1) PG8_BAR;
;     PG8_WAIT_V(2); PG8_BAR;
;     PG8_STAGE(PG8_SB(1, 0), cB + kstep, voffB); PG8_STAGE(PG8_SA(1, 0), cA + kstep, voffA); PG8_STAGE(PG8_SB(1, 1), cB + hB + kstep, voffB);
;     PG8_WAIT_V(6); PG8_BAR;
.LBB0_974:
	v_lshrrev_b32_e32 v16, 1, v14
	v_and_b32_e32 v16, 24, v16
	v_and_b32_e32 v15, 15, v14
	v_lshlrev_b32_e32 v17, 1, v16
	v_lshlrev_b32_e32 v14, 2, v14
	s_lshl_b32 s15, s15, 5
	v_lshl_or_b32 v140, s19, 6, v15
	v_lshl_or_b32 v15, v15, 6, v17
	s_lshl_b32 s19, s19, 13
	v_and_b32_e32 v14, 32, v14
	s_and_b32 s28, s15, 0x60
	s_add_i32 m0, s10, 0x18000
	v_lshl_add_u64 v[6:7], v[6:7], 0, s[62:63]
	v_bitop3_b32 v17, v15, s19, v14 bitop3:0xde
	s_lshl_b32 s15, s28, 7
	s_waitcnt vmcnt(2)
	s_barrier
	global_load_lds_dwordx4 v[6:7], off
	v_lshl_add_u64 v[4:5], v[4:5], 0, s[62:63]
	s_add_i32 m0, s10, 0x1a000
	s_add_i32 s19, s10, 0x8000
	s_add_i32 s26, s10, 0xa000
	global_load_lds_dwordx4 v[4:5], off
	v_lshl_add_u64 v[0:1], v[0:1], 0, s[62:63]
	s_mov_b32 m0, s19
	s_add_u32 s20, s52, 0x40080
	global_load_lds_dwordx4 v[0:1], off
	v_lshl_add_u64 v[0:1], v[2:3], 0, s[62:63]
	s_mov_b32 m0, s26
	s_addc_u32 s21, s53, 0
	global_load_lds_dwordx4 v[0:1], off
	s_add_i32 m0, s10, 0x1c000
	v_lshl_add_u64 v[0:1], s[20:21], 0, v[96:97]
	global_load_lds_dwordx4 v[0:1], off
	v_lshl_add_u64 v[0:1], s[20:21], 0, v[130:131]
	s_add_i32 m0, s10, 0x1e000
	s_cmpk_lt_u32 s14, 0x100
	global_load_lds_dwordx4 v[0:1], off
	v_lshlrev_b32_e32 v0, 14, v12
	v_and_b32_e32 v0, 0xffff8000, v0
	v_lshl_add_u32 v0, v11, 11, v0
	v_and_b32_e32 v1, 1, v12
	v_lshl_or_b32 v0, v1, 6, v0
	v_lshl_add_u32 v136, v13, 1, v0
	v_lshlrev_b32_e32 v0, 14, v8
	v_and_b32_e32 v0, 0xffff8000, v0
	s_waitcnt vmcnt(6)
	v_lshl_add_u32 v0, v9, 11, v0
	v_and_b32_e32 v1, 1, v8
	v_lshl_or_b32 v0, v1, 6, v0
	v_readlane_b32 s20, v255, 7
	v_bitop3_b32 v141, v15, s15, v14 bitop3:0xde
	s_cselect_b64 s[14:15], -1, 0
	s_waitcnt lgkmcnt(0)
	s_ashr_i32 s27, s18, 31
	v_or_b32_e32 v142, s28, v16
	v_mov_b32_e32 v137, v97
	v_lshl_add_u32 v138, v10, 1, v0
	v_mov_b32_e32 v139, v97
	s_mov_b32 s28, 0
	v_add_u32_e32 v143, 0, v17
	v_readlane_b32 s34, v254, 54
	s_mov_b32 s35, s20
	s_barrier
	v_readlane_b32 s21, v255, 8
	s_mov_b32 s100, 0
	s_branch .LBB0_977

;     __device__ bool next(int i, Unit& u) const { const long L = (long)i * G + c; if (L >= nwg) return false; tile_of((int)L, nM, nN, u.pm, u.pn, wgm); u.z = 0; return true; }
;     __device__ bool next(int i, Unit& u) const { const int j = i / 6, r = i - 6 * j; const long L = (long)j * G + c; if (L >= nwg) return false; tile_of((int)L, nM, nN, u.pm, u.pn, wgm); u.z = (r >> 1) + 4 * (r & 1); return true; }
; template <class Epi, class Sched, bool ALIGN_EPI = true>
; __device__ __forceinline__ void gemm_phase(PG8_LAS unsigned char* lds, const Gemm g, const Sched& S, const Epi& E) {
;     ...
;         const bool has_next = S.next(ui + 1, nxt);
;         const char* nA = has_next ? (const char*)(g.A + (long)nxt.z * g.zA) + (size_t)nxt.pm * tA : cA; const char* nB = has_next ? (const char*)(g.Bt + (long)nxt.z * g.zB) + (size_t)nxt.pn * tB : cB;
;     ...
; #pragma unroll
;         for (int a = 0; a < 2; ++a)
; #pragma unroll
;             for (int b = 0; b < 2; ++b)
; #pragma unroll
;                 for (int m = 0; m < 4; ++m)
; #pragma unroll
;                     for (int n = 0; n < 2; ++n) acc[a][b][m][n] = (f32x4){0.f, 0.f, 0.f, 0.f};
;         cur = nxt; cA = nA; cB = nB; ++ui;
.LBB0_979:
	s_ashr_i32 s41, s40, 31
	s_lshl_b64 s[36:37], s[40:41], 19
	s_add_u32 s42, s2, s36
	s_addc_u32 s43, s3, s37
	s_and_b64 s[36:37], s[38:39], exec
	s_cselect_b32 s36, s43, s51
	s_cselect_b32 s37, s42, s50
	s_ashr_i32 s21, s20, 31
	s_lshl_b64 s[44:45], s[20:21], 19
	s_add_u32 s46, s4, s44
	s_addc_u32 s47, s5, s45
	s_and_b64 s[44:45], s[38:39], exec
	s_cselect_b32 s21, s47, s53
	s_cselect_b32 s41, s46, s52
	s_add_u32 s50, s50, 0x40080
	s_addc_u32 s51, s51, 0
	s_add_u32 s44, s52, 0x100
	v_mov_b32_e32 v0, 0
	s_addc_u32 s45, s53, 0
	s_mov_b32 s56, -2
	v_mov_b32_e32 v1, v0
	v_mov_b32_e32 v2, v0
	v_mov_b32_e32 v3, v0
	v_mov_b32_e32 v4, v0
	v_mov_b32_e32 v5, v0
	v_mov_b32_e32 v6, v0
	v_mov_b32_e32 v7, v0
	v_mov_b32_e32 v8, v0
	v_mov_b32_e32 v9, v0
	v_mov_b32_e32 v10, v0
	v_mov_b32_e32 v11, v0
	v_mov_b32_e32 v12, v0
	v_mov_b32_e32 v13, v0
	v_mov_b32_e32 v14, v0
	v_mov_b32_e32 v15, v0
	v_mov_b32_e32 v24, v0
	v_mov_b32_e32 v25, v0
	v_mov_b32_e32 v26, v0
	v_mov_b32_e32 v27, v0
	v_mov_b32_e32 v28, v0
	v_mov_b32_e32 v29, v0
	v_mov_b32_e32 v30, v0
	v_mov_b32_e32 v31, v0
	v_mov_b32_e32 v40, v0
	v_mov_b32_e32 v41, v0
	v_mov_b32_e32 v42, v0
	v_mov_b32_e32 v43, v0
	v_mov_b32_e32 v44, v0
	v_mov_b32_e32 v45, v0
	v_mov_b32_e32 v46, v0
	v_mov_b32_e32 v47, v0
	v_mov_b32_e32 v16, v0
	v_mov_b32_e32 v17, v0
	v_mov_b32_e32 v18, v0
	v_mov_b32_e32 v19, v0
	v_mov_b32_e32 v20, v0
	v_mov_b32_e32 v21, v0
	v_mov_b32_e32 v22, v0
	v_mov_b32_e32 v23, v0
	v_mov_b32_e32 v32, v0
	v_mov_b32_e32 v33, v0
	v_mov_b32_e32 v34, v0
	v_mov_b32_e32 v35, v0
	v_mov_b32_e32 v36, v0
	v_mov_b32_e32 v37, v0
	v_mov_b32_e32 v38, v0
	v_mov_b32_e32 v39, v0
	v_mov_b32_e32 v48, v0
	v_mov_b32_e32 v49, v0
	v_mov_b32_e32 v50, v0
	v_mov_b32_e32 v51, v0
	v_mov_b32_e32 v52, v0
	v_mov_b32_e32 v53, v0
	v_mov_b32_e32 v54, v0
	v_mov_b32_e32 v55, v0
	v_mov_b32_e32 v56, v0
	v_mov_b32_e32 v57, v0
	v_mov_b32_e32 v58, v0
	v_mov_b32_e32 v59, v0
	v_mov_b32_e32 v60, v0
	v_mov_b32_e32 v61, v0
	v_mov_b32_e32 v62, v0
	v_mov_b32_e32 v63, v0
	v_mov_b32_e32 v64, v0
	v_mov_b32_e32 v65, v0
	v_mov_b32_e32 v66, v0
	v_mov_b32_e32 v67, v0
	v_mov_b32_e32 v68, v0
	v_mov_b32_e32 v69, v0
	v_mov_b32_e32 v70, v0
	v_mov_b32_e32 v71, v0
	v_mov_b32_e32 v72, v0
	v_mov_b32_e32 v73, v0
	v_mov_b32_e32 v74, v0
	v_mov_b32_e32 v75, v0
	v_mov_b32_e32 v76, v0
	v_mov_b32_e32 v77, v0
	v_mov_b32_e32 v78, v0
	v_mov_b32_e32 v79, v0
	v_mov_b32_e32 v88, v0
	v_mov_b32_e32 v89, v0
	v_mov_b32_e32 v90, v0
	v_mov_b32_e32 v91, v0
	v_mov_b32_e32 v92, v0
	v_mov_b32_e32 v93, v0
	v_mov_b32_e32 v94, v0
	v_mov_b32_e32 v95, v0
	v_mov_b32_e32 v106, v0
	v_mov_b32_e32 v107, v0
	v_mov_b32_e32 v108, v0
	v_mov_b32_e32 v109, v0
	v_mov_b32_e32 v110, v0
	v_mov_b32_e32 v111, v0
	v_mov_b32_e32 v112, v0
	v_mov_b32_e32 v113, v0
	v_mov_b32_e32 v80, v0
	v_mov_b32_e32 v81, v0
	v_mov_b32_e32 v82, v0
	v_mov_b32_e32 v83, v0
	v_mov_b32_e32 v84, v0
	v_mov_b32_e32 v85, v0
	v_mov_b32_e32 v86, v0
	v_mov_b32_e32 v87, v0
	v_mov_b32_e32 v98, v0
	v_mov_b32_e32 v99, v0
	v_mov_b32_e32 v100, v0
	v_mov_b32_e32 v101, v0
	v_mov_b32_e32 v102, v0
	v_mov_b32_e32 v103, v0
	v_mov_b32_e32 v104, v0
	v_mov_b32_e32 v105, v0
	v_mov_b32_e32 v114, v0
	v_mov_b32_e32 v115, v0
	v_mov_b32_e32 v116, v0
	v_mov_b32_e32 v117, v0
	v_mov_b32_e32 v118, v0
	v_mov_b32_e32 v119, v0
	v_mov_b32_e32 v120, v0
	v_mov_b32_e32 v121, v0
	v_mov_b32_e32 v122, v0
	v_mov_b32_e32 v123, v0
	v_mov_b32_e32 v124, v0
	v_mov_b32_e32 v125, v0
	v_mov_b32_e32 v126, v0
	v_mov_b32_e32 v127, v0
	v_mov_b32_e32 v128, v0
	v_mov_b32_e32 v129, v0
	s_cmp_eq_u32 s100, 1
	s_cbranch_scc1 .Lpeel_proj

; #define PG8_STAGE(bufoff, gbase, voff) do { _Pragma("unroll") for (int _i = 0; _i < 2; ++_i) \
;         __builtin_amdgcn_global_load_lds((const unsigned*)((const char*)(gbase) + (voff)[_i]), (PG8_LAS unsigned*)(lds + (bufoff) + ldsw + _i * 8192), 16, 0, 0); } while (0)
; #define PG8_LDA(dst, b, h) do { _Pragma("unroll") for (int m = 0; m < 4; ++m) _Pragma("unroll") for (int k = 0; k < 2; ++k) dst[m][k] = *(const PG8_LAS s16x8*)(lds + PG8_SA(b, h) + aoff + m * 2048 + k * 1024); } while (0)
; #define PG8_LDB(dst, b, h) do { _Pragma("unroll") for (int n = 0; n < 2; ++n) _Pragma("unroll") for (int k = 0; k < 2; ++k) dst[n][k] = *(const PG8_LAS s16x8*)(lds + PG8_SB(b, h) + boff + n * 2048 + k * 1024); } while (0)
; #define PG8_WAIT_V(n) asm volatile("s_waitcnt vmcnt(" #n ")" ::: "memory")
; #define PG8_WAIT_L(n) asm volatile("s_waitcnt lgkmcnt(" #n ")" ::: "memory")
; #define PG8_BAR __builtin_amdgcn_s_barrier()
; #define PG8_SCHED __builtin_amdgcn_sched_barrier(0)
; #define PG8_WAIT_V(n) asm volatile("s_waitcnt vmcnt(" #n ")" ::: "memory")
; template <class Epi, class Sched, bool ALIGN_EPI = true>
; __device__ __forceinline__ void gemm_phase(PG8_LAS unsigned char* lds, const Gemm g, const Sched& S, const Epi& E) {
;     ...
;             PG8_LDB(B0, 0, 0); PG8_LDB(B1, 0, 1); PG8_SCHED; PG8_LDA(At, 0, 0); PG8_STAGE(PG8_SA(1, 1), a1 + hA, voffA);
;             PG8_WAIT_V(8); PG8_WAIT_L(0); PG8_BAR; PG8_MMA(0, 0, At, B0); PG8_MMA(0, 1, At, B1); PG8_BAR; PG8_SCHED;
;             PG8_LDA(At, 0, 1); PG8_STAGE(PG8_SB(0, 0), b2, voffB); PG8_STAGE(PG8_SB(0, 1), b2 + hB, voffB); PG8_STAGE(PG8_SA(0, 0), a2, voffA);
;             PG8_WAIT_V(8); PG8_WAIT_L(0); PG8_BAR; PG8_MMA(1, 0, At, B0); PG8_MMA(1, 1, At, B1); PG8_BAR; PG8_SCHED;
;             PG8_LDB(B0, 1, 0); PG8_LDB(B1, 1, 1); PG8_SCHED; PG8_LDA(At, 1, 0); PG8_STAGE(PG8_SA(0, 1), a2 + hA, voffA);
;             PG8_WAIT_V(8); PG8_WAIT_L(0); PG8_BAR; PG8_MMA(0, 0, At, B0); PG8_MMA(0, 1, At, B1); PG8_BAR; PG8_SCHED;
;             PG8_LDA(At, 1, 1); PG8_STAGE(PG8_SB(1, 0), b3, voffB); PG8_STAGE(PG8_SB(1, 1), b3 + hB, voffB); PG8_STAGE(PG8_SA(1, 0), a3, voffA);
;             PG8_WAIT_V(8); PG8_WAIT_L(0); PG8_BAR; PG8_MMA(1, 0, At, B0); PG8_MMA(1, 1, At, B1); PG8_BAR; PG8_SCHED;
;         }
;         if constexpr (ALIGN_EPI) { if (wr == 0) PG8_BAR; }
;         if constexpr (!Epi::AFTER_DRAIN) E(acc, cur, wr, wc, fr, fq);
.LBB0_983:
	s_and_b64 vcc, exec, s[38:39]
	s_cbranch_vccz .Lproj_noprestage
	s_mov_b32 s100, 1
	s_add_u32 s52, s42, 0x40080
	s_addc_u32 s53, s43, 0
	v_lshl_add_u64 v[216:217], s[52:53], 0, v[136:137]
	s_add_i32 m0, s10, 0xc000
	s_nop 0
	global_load_lds_dwordx4 v[216:217], off
	v_lshl_add_u64 v[216:217], s[52:53], 0, v[138:139]
	s_add_i32 m0, s10, 0xe000
	s_nop 0
	global_load_lds_dwordx4 v[216:217], off

; #define PG8_STAGE(bufoff, gbase, voff) do { _Pragma("unroll") for (int _i = 0; _i < 2; ++_i) \
;         __builtin_amdgcn_global_load_lds((const unsigned*)((const char*)(gbase) + (voff)[_i]), (PG8_LAS unsigned*)(lds + (bufoff) + ldsw + _i * 8192), 16, 0, 0); } while (0)
; #define PG8_LDA(dst, b, h) do { _Pragma("unroll") for (int m = 0; m < 4; ++m) _Pragma("unroll") for (int k = 0; k < 2; ++k) dst[m][k] = *(const PG8_LAS s16x8*)(lds + PG8_SA(b, h) + aoff + m * 2048 + k * 1024); } while (0)
; #define PG8_LDB(dst, b, h) do { _Pragma("unroll") for (int n = 0; n < 2; ++n) _Pragma("unroll") for (int k = 0; k < 2; ++k) dst[n][k] = *(const PG8_LAS s16x8*)(lds + PG8_SB(b, h) + boff + n * 2048 + k * 1024); } while (0)
; #define PG8_WAIT_V(n) asm volatile("s_waitcnt vmcnt(" #n ")" ::: "memory")
; #define PG8_WAIT_L(n) asm volatile("s_waitcnt lgkmcnt(" #n ")" ::: "memory")
; #define PG8_BAR __builtin_amdgcn_s_barrier()
; #define PG8_SCHED __builtin_amdgcn_sched_barrier(0)
; #define PG8_STAGE(bufoff, gbase, voff) do { _Pragma("unroll") for (int _i = 0; _i < 2; ++_i) \
;         __builtin_amdgcn_global_load_lds((const unsigned*)((const char*)(gbase) + (voff)[_i]), (PG8_LAS unsigned*)(lds + (bufoff) + ldsw + _i * 8192), 16, 0, 0); } while (0)
; #define PG8_WAIT_V(n) asm volatile("s_waitcnt vmcnt(" #n ")" ::: "memory")
; template <class Epi, class Sched, bool ALIGN_EPI = true>
; __device__ __forceinline__ void gemm_phase(PG8_LAS unsigned char* lds, const Gemm g, const Sched& S, const Epi& E) {
;     ...
;         for (int t = 0; t < nt; t += 2) {
;             const bool last = (t == nt - 2);
;             const char* a1 = cA + (size_t)(t + 1) * kstep;
;             const char* a2 = last ? nA : cA + (size_t)(t + 2) * kstep; const char* b2 = last ? nB : cB + (size_t)(t + 2) * kstep;
;             const char* a3 = a2 + kstep; const char* b3 = b2 + kstep;
;             PG8_LDB(B0, 0, 0); PG8_LDB(B1, 0, 1); PG8_SCHED; PG8_LDA(At, 0, 0); PG8_STAGE(PG8_SA(1, 1), a1 + hA, voffA);
;             PG8_WAIT_V(8); PG8_WAIT_L(0); PG8_BAR; PG8_MMA(0, 0, At, B0); PG8_MMA(0, 1, At, B1); PG8_BAR; PG8_SCHED;
;             PG8_LDA(At, 0, 1); PG8_STAGE(PG8_SB(0, 0), b2, voffB); PG8_STAGE(PG8_SB(0, 1), b2 + hB, voffB); PG8_STAGE(PG8_SA(0, 0), a2, voffA);
;             PG8_WAIT_V(8); PG8_WAIT_L(0); PG8_BAR; PG8_MMA(1, 0, At, B0); PG8_MMA(1, 1, At, B1); PG8_BAR; PG8_SCHED;
.Lpeel_proj:
	s_add_u32 s52, s50, 0xfffc0080
	s_addc_u32 s53, s51, -1
	s_add_i32 s57, 0, 0x10000
	s_cmp_eq_u32 s56, 12
	s_cselect_b32 s55, s36, s53
	s_cselect_b32 s54, s37, s52
	s_cselect_b32 s53, s21, s45
	s_cselect_b32 s52, s41, s44
	s_add_i32 s60, 0, 0x14000
	v_add_u32_e32 v156, s57, v141
	v_add_u32_e32 v172, s60, v141
	ds_read_b128 v[144:147], v156
	ds_read_b128 v[148:151], v156 offset:1024
	ds_read_b128 v[152:155], v156 offset:2048
	ds_read_b128 v[156:159], v156 offset:3072
	ds_read_b128 v[160:163], v172
	ds_read_b128 v[164:167], v172 offset:1024
	ds_read_b128 v[168:171], v172 offset:2048
	ds_read_b128 v[172:175], v172 offset:3072
	ds_read_b128 v[176:179], v143
	ds_read_b128 v[180:183], v143 offset:1024
	ds_read_b128 v[184:187], v143 offset:2048
	ds_read_b128 v[188:191], v143 offset:3072
	ds_read_b128 v[192:195], v143 offset:4096
	ds_read_b128 v[196:199], v143 offset:5120
	ds_read_b128 v[200:203], v143 offset:6144
	ds_read_b128 v[204:207], v143 offset:7168
	s_waitcnt vmcnt(24)
	s_waitcnt lgkmcnt(0)
	s_barrier
	s_setprio 1
	s_waitcnt lgkmcnt(0)
	v_mfma_f32_16x16x32_f16 v[126:129], v[144:147], v[176:179], v[126:129]
	v_mfma_f32_16x16x32_f16 v[122:125], v[152:155], v[176:179], v[122:125]
	v_mfma_f32_16x16x32_f16 v[118:121], v[144:147], v[184:187], v[118:121]
	v_mfma_f32_16x16x32_f16 v[114:117], v[152:155], v[184:187], v[114:117]
	v_mfma_f32_16x16x32_f16 v[102:105], v[144:147], v[192:195], v[102:105]
	v_mfma_f32_16x16x32_f16 v[98:101], v[152:155], v[192:195], v[98:101]
	v_mfma_f32_16x16x32_f16 v[84:87], v[144:147], v[200:203], v[84:87]
	v_mfma_f32_16x16x32_f16 v[80:83], v[152:155], v[200:203], v[80:83]
	v_mfma_f32_16x16x32_f16 v[126:129], v[148:151], v[180:183], v[126:129]
	v_mfma_f32_16x16x32_f16 v[122:125], v[156:159], v[180:183], v[122:125]
	v_mfma_f32_16x16x32_f16 v[118:121], v[148:151], v[188:191], v[118:121]
	v_mfma_f32_16x16x32_f16 v[114:117], v[156:159], v[188:191], v[114:117]
	v_mfma_f32_16x16x32_f16 v[102:105], v[148:151], v[196:199], v[102:105]
	v_mfma_f32_16x16x32_f16 v[98:101], v[156:159], v[196:199], v[98:101]
	v_mfma_f32_16x16x32_f16 v[84:87], v[148:151], v[204:207], v[84:87]
	v_mfma_f32_16x16x32_f16 v[80:83], v[156:159], v[204:207], v[80:83]
	s_setprio 0
	s_setprio 1
	v_mfma_f32_16x16x32_f16 v[110:113], v[160:163], v[176:179], v[110:113]
	v_mfma_f32_16x16x32_f16 v[106:109], v[168:171], v[176:179], v[106:109]
	v_mfma_f32_16x16x32_f16 v[92:95], v[160:163], v[184:187], v[92:95]
	v_mfma_f32_16x16x32_f16 v[88:91], v[168:171], v[184:187], v[88:91]
	v_mfma_f32_16x16x32_f16 v[76:79], v[160:163], v[192:195], v[76:79]
	v_mfma_f32_16x16x32_f16 v[72:75], v[168:171], v[192:195], v[72:75]
	v_mfma_f32_16x16x32_f16 v[68:71], v[160:163], v[200:203], v[68:71]
	v_mfma_f32_16x16x32_f16 v[64:67], v[168:171], v[200:203], v[64:67]
	v_mfma_f32_16x16x32_f16 v[110:113], v[164:167], v[180:183], v[110:113]
	v_mfma_f32_16x16x32_f16 v[106:109], v[172:175], v[180:183], v[106:109]
	v_mfma_f32_16x16x32_f16 v[92:95], v[164:167], v[188:191], v[92:95]
	v_mfma_f32_16x16x32_f16 v[88:91], v[172:175], v[188:191], v[88:91]
	v_mfma_f32_16x16x32_f16 v[76:79], v[164:167], v[196:199], v[76:79]
	v_mfma_f32_16x16x32_f16 v[72:75], v[172:175], v[196:199], v[72:75]
	v_mfma_f32_16x16x32_f16 v[68:71], v[164:167], v[204:207], v[68:71]
	v_mfma_f32_16x16x32_f16 v[64:67], v[172:175], v[204:207], v[64:67]
	s_setprio 0
	s_barrier
	s_add_i32 s57, s57, s6
	v_lshl_add_u64 v[208:209], s[52:53], 0, v[96:97]
	s_mov_b32 m0, s57
	ds_read_b128 v[176:179], v143 offset:16384
	ds_read_b128 v[180:183], v143 offset:17408
	ds_read_b128 v[184:187], v143 offset:18432
	ds_read_b128 v[188:191], v143 offset:19456
	ds_read_b128 v[192:195], v143 offset:20480
	ds_read_b128 v[196:199], v143 offset:21504
	ds_read_b128 v[200:203], v143 offset:22528
	ds_read_b128 v[204:207], v143 offset:23552
	global_load_lds_dwordx4 v[208:209], off
	s_add_i32 m0, s57, 0x2000
	s_add_u32 s58, s52, 0x40000
	v_lshl_add_u64 v[210:211], s[52:53], 0, v[130:131]
	s_addc_u32 s59, s53, 0
	s_add_i32 s57, s60, s6
	global_load_lds_dwordx4 v[210:211], off
	v_lshl_add_u64 v[212:213], s[58:59], 0, v[96:97]
	s_mov_b32 m0, s57
	v_lshl_add_u64 v[214:215], s[54:55], 0, v[132:133]
	global_load_lds_dwordx4 v[212:213], off
	v_lshl_add_u64 v[212:213], s[58:59], 0, v[130:131]
	s_add_i32 m0, s57, 0x2000
	s_nop 0
	global_load_lds_dwordx4 v[212:213], off
	v_lshl_add_u64 v[212:213], s[54:55], 0, v[134:135]
	s_mov_b32 m0, s10
	s_nop 0
	global_load_lds_dwordx4 v[212:213], off
	s_mov_b32 m0, s11
	s_nop 0
	global_load_lds_dwordx4 v[214:215], off
	s_waitcnt vmcnt(24)
	s_waitcnt lgkmcnt(0)
	s_barrier
; #define PG8_STAGE(bufoff, gbase, voff) do { _Pragma("unroll") for (int _i = 0; _i < 2; ++_i) \
;         __builtin_amdgcn_global_load_lds((const unsigned*)((const char*)(gbase) + (voff)[_i]), (PG8_LAS unsigned*)(lds + (bufoff) + ldsw + _i * 8192), 16, 0, 0); } while (0)
; #define PG8_LDA(dst, b, h) do { _Pragma("unroll") for (int m = 0; m < 4; ++m) _Pragma("unroll") for (int k = 0; k < 2; ++k) dst[m][k] = *(const PG8_LAS s16x8*)(lds + PG8_SA(b, h) + aoff + m * 2048 + k * 1024); } while (0)
; #define PG8_LDB(dst, b, h) do { _Pragma("unroll") for (int n = 0; n < 2; ++n) _Pragma("unroll") for (int k = 0; k < 2; ++k) dst[n][k] = *(const PG8_LAS s16x8*)(lds + PG8_SB(b, h) + boff + n * 2048 + k * 1024); } while (0)
; #define PG8_WAIT_V(n) asm volatile("s_waitcnt vmcnt(" #n ")" ::: "memory")
; #define PG8_WAIT_L(n) asm volatile("s_waitcnt lgkmcnt(" #n ")" ::: "memory")
; #define PG8_BAR __builtin_amdgcn_s_barrier()
; #define PG8_SCHED __builtin_amdgcn_sched_barrier(0)
; #define PG8_STAGE(bufoff, gbase, voff) do { _Pragma("unroll") for (int _i = 0; _i < 2; ++_i) \
;         __builtin_amdgcn_global_load_lds((const unsigned*)((const char*)(gbase) + (voff)[_i]), (PG8_LAS unsigned*)(lds + (bufoff) + ldsw + _i * 8192), 16, 0, 0); } while (0)
; #define PG8_LDA(dst, b, h) do { _Pragma("unroll") for (int m = 0; m < 4; ++m) _Pragma("unroll") for (int k = 0; k < 2; ++k) dst[m][k] = *(const PG8_LAS s16x8*)(lds + PG8_SA(b, h) + aoff + m * 2048 + k * 1024); } while (0)
; #define PG8_LDB(dst, b, h) do { _Pragma("unroll") for (int n = 0; n < 2; ++n) _Pragma("unroll") for (int k = 0; k < 2; ++k) dst[n][k] = *(const PG8_LAS s16x8*)(lds + PG8_SB(b, h) + boff + n * 2048 + k * 1024); } while (0)
; #define PG8_WAIT_V(n) asm volatile("s_waitcnt vmcnt(" #n ")" ::: "memory")
; #define PG8_WAIT_L(n) asm volatile("s_waitcnt lgkmcnt(" #n ")" ::: "memory")
; template <class Epi, class Sched, bool ALIGN_EPI = true>
; __device__ __forceinline__ void gemm_phase(PG8_LAS unsigned char* lds, const Gemm g, const Sched& S, const Epi& E) {
;     ...
;             PG8_WAIT_V(8); PG8_WAIT_L(0); PG8_BAR; PG8_MMA(1, 0, At, B0); PG8_MMA(1, 1, At, B1); PG8_BAR; PG8_SCHED;
;             PG8_LDB(B0, 1, 0); PG8_LDB(B1, 1, 1); PG8_SCHED; PG8_LDA(At, 1, 0); PG8_STAGE(PG8_SA(0, 1), a2 + hA, voffA);
;             PG8_WAIT_V(8); PG8_WAIT_L(0); PG8_BAR; PG8_MMA(0, 0, At, B0); PG8_MMA(0, 1, At, B1); PG8_BAR; PG8_SCHED;
	s_setprio 1
	s_waitcnt lgkmcnt(0)
	v_mfma_f32_16x16x32_f16 v[60:63], v[144:147], v[176:179], v[60:63]
	v_mfma_f32_16x16x32_f16 v[56:59], v[152:155], v[176:179], v[56:59]
	v_mfma_f32_16x16x32_f16 v[52:55], v[144:147], v[184:187], v[52:55]
	v_mfma_f32_16x16x32_f16 v[48:51], v[152:155], v[184:187], v[48:51]
	v_mfma_f32_16x16x32_f16 v[36:39], v[144:147], v[192:195], v[36:39]
	v_mfma_f32_16x16x32_f16 v[32:35], v[152:155], v[192:195], v[32:35]
	v_mfma_f32_16x16x32_f16 v[20:23], v[144:147], v[200:203], v[20:23]
	v_mfma_f32_16x16x32_f16 v[16:19], v[152:155], v[200:203], v[16:19]
	v_mfma_f32_16x16x32_f16 v[60:63], v[148:151], v[180:183], v[60:63]
	v_mfma_f32_16x16x32_f16 v[56:59], v[156:159], v[180:183], v[56:59]
	v_mfma_f32_16x16x32_f16 v[52:55], v[148:151], v[188:191], v[52:55]
	v_mfma_f32_16x16x32_f16 v[48:51], v[156:159], v[188:191], v[48:51]
	v_mfma_f32_16x16x32_f16 v[36:39], v[148:151], v[196:199], v[36:39]
	v_mfma_f32_16x16x32_f16 v[32:35], v[156:159], v[196:199], v[32:35]
	v_mfma_f32_16x16x32_f16 v[20:23], v[148:151], v[204:207], v[20:23]
	v_mfma_f32_16x16x32_f16 v[16:19], v[156:159], v[204:207], v[16:19]
	s_setprio 0
	s_setprio 1
	v_mfma_f32_16x16x32_f16 v[44:47], v[160:163], v[176:179], v[44:47]
	v_mfma_f32_16x16x32_f16 v[40:43], v[168:171], v[176:179], v[40:43]
	v_mfma_f32_16x16x32_f16 v[28:31], v[160:163], v[184:187], v[28:31]
	v_mfma_f32_16x16x32_f16 v[24:27], v[168:171], v[184:187], v[24:27]
	v_mfma_f32_16x16x32_f16 v[12:15], v[160:163], v[192:195], v[12:15]
	v_mfma_f32_16x16x32_f16 v[8:11], v[168:171], v[192:195], v[8:11]
	v_mfma_f32_16x16x32_f16 v[4:7], v[160:163], v[200:203], v[4:7]
	v_mfma_f32_16x16x32_f16 v[0:3], v[168:171], v[200:203], v[0:3]
	v_mfma_f32_16x16x32_f16 v[44:47], v[164:167], v[180:183], v[44:47]
	v_mfma_f32_16x16x32_f16 v[40:43], v[172:175], v[180:183], v[40:43]
	v_mfma_f32_16x16x32_f16 v[28:31], v[164:167], v[188:191], v[28:31]
	v_mfma_f32_16x16x32_f16 v[24:27], v[172:175], v[188:191], v[24:27]
	v_mfma_f32_16x16x32_f16 v[12:15], v[164:167], v[196:199], v[12:15]
	v_mfma_f32_16x16x32_f16 v[8:11], v[172:175], v[196:199], v[8:11]
	v_mfma_f32_16x16x32_f16 v[4:7], v[164:167], v[204:207], v[4:7]
	v_mfma_f32_16x16x32_f16 v[0:3], v[172:175], v[204:207], v[0:3]
	s_setprio 0
	s_barrier
	s_add_i32 s57, 0, 0x18000
	s_add_i32 s58, 0, 0x1c000
	v_add_u32_e32 v156, s57, v141
	v_add_u32_e32 v172, s58, v141
	ds_read_b128 v[144:147], v156
	ds_read_b128 v[148:151], v156 offset:1024
	ds_read_b128 v[152:155], v156 offset:2048
	ds_read_b128 v[156:159], v156 offset:3072
	ds_read_b128 v[160:163], v172
	ds_read_b128 v[164:167], v172 offset:1024
	ds_read_b128 v[168:171], v172 offset:2048
	ds_read_b128 v[172:175], v172 offset:3072
	s_add_u32 s54, s54, 0x40000
	s_addc_u32 s55, s55, 0
	s_mov_b32 m0, s12
	v_lshl_add_u64 v[216:217], s[54:55], 0, v[134:135]
	ds_read_b128 v[176:179], v143 offset:32768
	ds_read_b128 v[180:183], v143 offset:33792
	ds_read_b128 v[184:187], v143 offset:34816
	ds_read_b128 v[188:191], v143 offset:35840
	ds_read_b128 v[192:195], v143 offset:36864
	ds_read_b128 v[196:199], v143 offset:37888
	ds_read_b128 v[200:203], v143 offset:38912
	ds_read_b128 v[204:207], v143 offset:39936
	global_load_lds_dwordx4 v[216:217], off
	v_lshl_add_u64 v[216:217], s[54:55], 0, v[132:133]
	s_mov_b32 m0, s13
	s_nop 0
	global_load_lds_dwordx4 v[216:217], off
	s_waitcnt vmcnt(24)
	s_waitcnt lgkmcnt(0)
	s_barrier
	s_setprio 1
	s_waitcnt lgkmcnt(0)
	v_mfma_f32_16x16x32_f16 v[126:129], v[144:147], v[176:179], v[126:129]
	v_mfma_f32_16x16x32_f16 v[122:125], v[152:155], v[176:179], v[122:125]
	v_mfma_f32_16x16x32_f16 v[118:121], v[144:147], v[184:187], v[118:121]
	v_mfma_f32_16x16x32_f16 v[114:117], v[152:155], v[184:187], v[114:117]
	v_mfma_f32_16x16x32_f16 v[102:105], v[144:147], v[192:195], v[102:105]
	v_mfma_f32_16x16x32_f16 v[98:101], v[152:155], v[192:195], v[98:101]
	v_mfma_f32_16x16x32_f16 v[84:87], v[144:147], v[200:203], v[84:87]
	v_mfma_f32_16x16x32_f16 v[80:83], v[152:155], v[200:203], v[80:83]
	v_mfma_f32_16x16x32_f16 v[126:129], v[148:151], v[180:183], v[126:129]
	v_mfma_f32_16x16x32_f16 v[122:125], v[156:159], v[180:183], v[122:125]
	v_mfma_f32_16x16x32_f16 v[118:121], v[148:151], v[188:191], v[118:121]
	v_mfma_f32_16x16x32_f16 v[114:117], v[156:159], v[188:191], v[114:117]
	v_mfma_f32_16x16x32_f16 v[102:105], v[148:151], v[196:199], v[102:105]
	v_mfma_f32_16x16x32_f16 v[98:101], v[156:159], v[196:199], v[98:101]
	v_mfma_f32_16x16x32_f16 v[84:87], v[148:151], v[204:207], v[84:87]
	v_mfma_f32_16x16x32_f16 v[80:83], v[156:159], v[204:207], v[80:83]
	s_setprio 0
	s_setprio 1
	v_mfma_f32_16x16x32_f16 v[110:113], v[160:163], v[176:179], v[110:113]
	v_mfma_f32_16x16x32_f16 v[106:109], v[168:171], v[176:179], v[106:109]
	v_mfma_f32_16x16x32_f16 v[92:95], v[160:163], v[184:187], v[92:95]
	v_mfma_f32_16x16x32_f16 v[88:91], v[168:171], v[184:187], v[88:91]
	v_mfma_f32_16x16x32_f16 v[76:79], v[160:163], v[192:195], v[76:79]
	v_mfma_f32_16x16x32_f16 v[72:75], v[168:171], v[192:195], v[72:75]
	v_mfma_f32_16x16x32_f16 v[68:71], v[160:163], v[200:203], v[68:71]
	v_mfma_f32_16x16x32_f16 v[64:67], v[168:171], v[200:203], v[64:67]
	v_mfma_f32_16x16x32_f16 v[110:113], v[164:167], v[180:183], v[110:113]
	v_mfma_f32_16x16x32_f16 v[106:109], v[172:175], v[180:183], v[106:109]
	v_mfma_f32_16x16x32_f16 v[92:95], v[164:167], v[188:191], v[92:95]
	v_mfma_f32_16x16x32_f16 v[88:91], v[172:175], v[188:191], v[88:91]
	v_mfma_f32_16x16x32_f16 v[76:79], v[164:167], v[196:199], v[76:79]
	v_mfma_f32_16x16x32_f16 v[72:75], v[172:175], v[196:199], v[72:75]
	v_mfma_f32_16x16x32_f16 v[68:71], v[164:167], v[204:207], v[68:71]
	v_mfma_f32_16x16x32_f16 v[64:67], v[172:175], v[204:207], v[64:67]
	s_setprio 0
	s_barrier
; #define PG8_STAGE(bufoff, gbase, voff) do { _Pragma("unroll") for (int _i = 0; _i < 2; ++_i) \
;         __builtin_amdgcn_global_load_lds((const unsigned*)((const char*)(gbase) + (voff)[_i]), (PG8_LAS unsigned*)(lds + (bufoff) + ldsw + _i * 8192), 16, 0, 0); } while (0)
; #define PG8_LDA(dst, b, h) do { _Pragma("unroll") for (int m = 0; m < 4; ++m) _Pragma("unroll") for (int k = 0; k < 2; ++k) dst[m][k] = *(const PG8_LAS s16x8*)(lds + PG8_SA(b, h) + aoff + m * 2048 + k * 1024); } while (0)
; #define PG8_WAIT_V(n) asm volatile("s_waitcnt vmcnt(" #n ")" ::: "memory")
; #define PG8_WAIT_L(n) asm volatile("s_waitcnt lgkmcnt(" #n ")" ::: "memory")
; #define PG8_BAR __builtin_amdgcn_s_barrier()
; #define PG8_SCHED __builtin_amdgcn_sched_barrier(0)
; #define PG8_STAGE(bufoff, gbase, voff) do { _Pragma("unroll") for (int _i = 0; _i < 2; ++_i) \
;         __builtin_amdgcn_global_load_lds((const unsigned*)((const char*)(gbase) + (voff)[_i]), (PG8_LAS unsigned*)(lds + (bufoff) + ldsw + _i * 8192), 16, 0, 0); } while (0)
; #define PG8_LDA(dst, b, h) do { _Pragma("unroll") for (int m = 0; m < 4; ++m) _Pragma("unroll") for (int k = 0; k < 2; ++k) dst[m][k] = *(const PG8_LAS s16x8*)(lds + PG8_SA(b, h) + aoff + m * 2048 + k * 1024); } while (0)
; #define PG8_WAIT_V(n) asm volatile("s_waitcnt vmcnt(" #n ")" ::: "memory")
; #define PG8_WAIT_L(n) asm volatile("s_waitcnt lgkmcnt(" #n ")" ::: "memory")
; #define PG8_BAR __builtin_amdgcn_s_barrier()
; #define PG8_SCHED __builtin_amdgcn_sched_barrier(0)
; template <class Epi, class Sched, bool ALIGN_EPI = true>
; __device__ __forceinline__ void gemm_phase(PG8_LAS unsigned char* lds, const Gemm g, const Sched& S, const Epi& E) {
;     ...
;             PG8_LDA(At, 1, 1); PG8_STAGE(PG8_SB(1, 0), b3, voffB); PG8_STAGE(PG8_SB(1, 1), b3 + hB, voffB); PG8_STAGE(PG8_SA(1, 0), a3, voffA);
;             PG8_WAIT_V(8); PG8_WAIT_L(0); PG8_BAR; PG8_MMA(1, 0, At, B0); PG8_MMA(1, 1, At, B1); PG8_BAR; PG8_SCHED;
;         }
	s_add_i32 s54, s57, s6
	v_lshl_add_u64 v[208:209], v[208:209], 0, s[62:63]
	s_mov_b32 m0, s54
	ds_read_b128 v[176:179], v143 offset:49152
	ds_read_b128 v[180:183], v143 offset:50176
	ds_read_b128 v[184:187], v143 offset:51200
	ds_read_b128 v[188:191], v143 offset:52224
	ds_read_b128 v[192:195], v143 offset:53248
	ds_read_b128 v[196:199], v143 offset:54272
	ds_read_b128 v[200:203], v143 offset:55296
	ds_read_b128 v[204:207], v143 offset:56320
	global_load_lds_dwordx4 v[208:209], off
	s_add_i32 m0, s54, 0x2000
	s_add_u32 s52, s52, 0x40080
	v_lshl_add_u64 v[208:209], v[210:211], 0, s[62:63]
	s_addc_u32 s53, s53, 0
	s_add_i32 s54, s58, s6
	global_load_lds_dwordx4 v[208:209], off
	v_lshl_add_u64 v[208:209], s[52:53], 0, v[96:97]
	s_mov_b32 m0, s54
	s_nop 0
	global_load_lds_dwordx4 v[208:209], off
	v_lshl_add_u64 v[208:209], s[52:53], 0, v[130:131]
	s_add_i32 m0, s54, 0x2000
	s_nop 0
	global_load_lds_dwordx4 v[208:209], off
	v_lshl_add_u64 v[208:209], v[212:213], 0, s[62:63]
	s_mov_b32 m0, s19
	s_nop 0
	global_load_lds_dwordx4 v[208:209], off
	v_lshl_add_u64 v[208:209], v[214:215], 0, s[62:63]
	s_mov_b32 m0, s26
	s_nop 0
	global_load_lds_dwordx4 v[208:209], off
	s_waitcnt vmcnt(8)
	s_waitcnt lgkmcnt(0)
	s_barrier
	s_setprio 1
	s_waitcnt lgkmcnt(0)
	v_mfma_f32_16x16x32_f16 v[60:63], v[144:147], v[176:179], v[60:63]
	v_mfma_f32_16x16x32_f16 v[56:59], v[152:155], v[176:179], v[56:59]
	v_mfma_f32_16x16x32_f16 v[52:55], v[144:147], v[184:187], v[52:55]
	v_mfma_f32_16x16x32_f16 v[48:51], v[152:155], v[184:187], v[48:51]
	v_mfma_f32_16x16x32_f16 v[36:39], v[144:147], v[192:195], v[36:39]
	v_mfma_f32_16x16x32_f16 v[32:35], v[152:155], v[192:195], v[32:35]
	v_mfma_f32_16x16x32_f16 v[20:23], v[144:147], v[200:203], v[20:23]
	v_mfma_f32_16x16x32_f16 v[16:19], v[152:155], v[200:203], v[16:19]
	v_mfma_f32_16x16x32_f16 v[60:63], v[148:151], v[180:183], v[60:63]
	v_mfma_f32_16x16x32_f16 v[56:59], v[156:159], v[180:183], v[56:59]
	v_mfma_f32_16x16x32_f16 v[52:55], v[148:151], v[188:191], v[52:55]
	v_mfma_f32_16x16x32_f16 v[48:51], v[156:159], v[188:191], v[48:51]
	v_mfma_f32_16x16x32_f16 v[36:39], v[148:151], v[196:199], v[36:39]
	v_mfma_f32_16x16x32_f16 v[32:35], v[156:159], v[196:199], v[32:35]
	v_mfma_f32_16x16x32_f16 v[20:23], v[148:151], v[204:207], v[20:23]
	v_mfma_f32_16x16x32_f16 v[16:19], v[156:159], v[204:207], v[16:19]
	s_setprio 0
	s_setprio 1
	v_mfma_f32_16x16x32_f16 v[44:47], v[160:163], v[176:179], v[44:47]
	v_mfma_f32_16x16x32_f16 v[40:43], v[168:171], v[176:179], v[40:43]
	v_mfma_f32_16x16x32_f16 v[28:31], v[160:163], v[184:187], v[28:31]
	v_mfma_f32_16x16x32_f16 v[24:27], v[168:171], v[184:187], v[24:27]
	v_mfma_f32_16x16x32_f16 v[12:15], v[160:163], v[192:195], v[12:15]
	v_mfma_f32_16x16x32_f16 v[8:11], v[168:171], v[192:195], v[8:11]
	v_mfma_f32_16x16x32_f16 v[4:7], v[160:163], v[200:203], v[4:7]
	v_mfma_f32_16x16x32_f16 v[0:3], v[168:171], v[200:203], v[0:3]
	v_mfma_f32_16x16x32_f16 v[44:47], v[164:167], v[180:183], v[44:47]
	v_mfma_f32_16x16x32_f16 v[40:43], v[172:175], v[180:183], v[40:43]
	v_mfma_f32_16x16x32_f16 v[28:31], v[164:167], v[188:191], v[28:31]
	v_mfma_f32_16x16x32_f16 v[24:27], v[172:175], v[188:191], v[24:27]
	v_mfma_f32_16x16x32_f16 v[12:15], v[164:167], v[196:199], v[12:15]
	v_mfma_f32_16x16x32_f16 v[8:11], v[172:175], v[196:199], v[8:11]
	v_mfma_f32_16x16x32_f16 v[4:7], v[164:167], v[204:207], v[4:7]
	v_mfma_f32_16x16x32_f16 v[0:3], v[172:175], v[204:207], v[0:3]
	s_setprio 0
	s_barrier
	s_add_i32 s56, s56, 2
	s_add_u32 s50, s50, 0x100
	s_addc_u32 s51, s51, 0
	s_add_u32 s44, s44, 0x100
	s_addc_u32 s45, s45, 0
	s_cmp_gt_u32 s56, 13
	s_branch .LBB0_980

; __global__ void __launch_bounds__(NTHREADS, 2) mega(MArgs a) {
	.amdhsa_kernel _Z4mega5MArgs
		.amdhsa_group_segment_fixed_size 0
		.amdhsa_private_segment_fixed_size 0
		.amdhsa_kernarg_size 368
		.amdhsa_user_sgpr_count 2
		.amdhsa_user_sgpr_dispatch_ptr 0
		.amdhsa_user_sgpr_queue_ptr 0
		.amdhsa_user_sgpr_kernarg_segment_ptr 1
		.amdhsa_user_sgpr_dispatch_id 0
		.amdhsa_user_sgpr_kernarg_preload_length 0
		.amdhsa_user_sgpr_kernarg_preload_offset 0
		.amdhsa_user_sgpr_private_segment_size 0
		.amdhsa_uses_dynamic_stack 0
		.amdhsa_enable_private_segment 0
		.amdhsa_system_sgpr_workgroup_id_x 1
		.amdhsa_system_sgpr_workgroup_id_y 0
		.amdhsa_system_sgpr_workgroup_id_z 0
		.amdhsa_system_sgpr_workgroup_info 0
		.amdhsa_system_vgpr_workitem_id 2
		.amdhsa_next_free_vgpr 256
		.amdhsa_next_free_sgpr 102
		.amdhsa_accum_offset 256
		.amdhsa_reserve_vcc 1
		.amdhsa_float_round_mode_32 0
		.amdhsa_float_round_mode_16_64 0
		.amdhsa_float_denorm_mode_32 3
		.amdhsa_float_denorm_mode_16_64 3
		.amdhsa_dx10_clamp 1
		.amdhsa_ieee_mode 1
		.amdhsa_fp16_overflow 0
		.amdhsa_tg_split 0
		.amdhsa_exception_fp_ieee_invalid_op 0
		.amdhsa_exception_fp_denorm_src 0
		.amdhsa_exception_fp_ieee_div_zero 0
		.amdhsa_exception_fp_ieee_overflow 0
		.amdhsa_exception_fp_ieee_underflow 0
		.amdhsa_exception_fp_ieee_inexact 0
		.amdhsa_exception_int_div_zero 0
	.end_amdhsa_kernel

; __global__ void __launch_bounds__(NTHREADS, 2) mega(MArgs a) {
amdhsa.kernels:
  - .agpr_count:     0
    .args:
      - .offset:         0
        .size:           112
        .value_kind:     by_value
      - .offset:         112
        .size:           4
        .value_kind:     hidden_block_count_x
      - .offset:         116
        .size:           4
        .value_kind:     hidden_block_count_y
      - .offset:         120
        .size:           4
        .value_kind:     hidden_block_count_z
      - .offset:         124
        .size:           2
        .value_kind:     hidden_group_size_x
      - .offset:         126
        .size:           2
        .value_kind:     hidden_group_size_y
      - .offset:         128
        .size:           2
        .value_kind:     hidden_group_size_z
      - .offset:         130
        .size:           2
        .value_kind:     hidden_remainder_x
      - .offset:         132
        .size:           2
        .value_kind:     hidden_remainder_y
      - .offset:         134
        .size:           2
        .value_kind:     hidden_remainder_z
      - .offset:         152
        .size:           8
        .value_kind:     hidden_global_offset_x
      - .offset:         160
        .size:           8
        .value_kind:     hidden_global_offset_y
      - .offset:         168
        .size:           8
        .value_kind:     hidden_global_offset_z
      - .offset:         176
        .size:           2
        .value_kind:     hidden_grid_dims
      - .offset:         200
        .size:           8
        .value_kind:     hidden_multigrid_sync_arg
      - .offset:         232
        .size:           4
        .value_kind:     hidden_dynamic_lds_size
    .group_segment_fixed_size: 0
    .kernarg_segment_align: 8
    .kernarg_segment_size: 368
    .language:       OpenCL C
    .language_version:
      - 2
      - 0
    .max_flat_workgroup_size: 512
    .name:           _Z4mega5MArgs
    .private_segment_fixed_size: 0
    .sgpr_count:     108
    .sgpr_spill_count: 266
    .symbol:         _Z4mega5MArgs.kd
    .uniform_work_group_size: 1
    .uses_dynamic_stack: false
    .vgpr_count:     256
    .vgpr_spill_count: 0
    .wavefront_size: 64
